# M3: M2 + K3 prefetch of graph-1/2 PART rows and LSUM entries before the first load round (de-serialise the compiler's 3 dependent memory rounds)
# baseline (speedup 1.0000x reference)
_Z10epi_kernelPKDF16_PKfS2_S2_S2_S2_Pf:
	s_load_dwordx8 s[4:11], s[0:1], 0x0
	s_load_dwordx2 s[20:21], s[0:1], 0x20
	s_load_dwordx2 s[22:23], s[0:1], 0x30
	v_and_b32_e32 v55, 15, v0
	v_mov_b32_e32 v99, 0
	v_bfe_u32 v70, v0, 4, 2
	v_and_b32_e32 v2, 0xc0, v0
	v_lshl_or_b32 v16, v70, 3, v2
	v_lshlrev_b32_e32 v2, 10, v55
	v_mov_b32_e32 v3, v99
	v_lshrrev_b32_e32 v1, 6, v0
	s_waitcnt lgkmcnt(0)
	v_and_b32_e32 v128, 15, v0
	v_bfe_u32 v129, v0, 4, 2
	v_lshlrev_b32_e32 v130, 9, v128
	v_lshl_add_u32 v130, v1, 7, v130
	v_lshl_add_u32 v130, v129, 4, v130
	v_lshlrev_b32_e32 v131, 4, v128
	v_lshl_add_u32 v131, v1, 2, v131
	s_lshr_b32 s32, s2, 2
	s_and_b32 s33, s2, 3
	s_lshl_b32 s33, s33, 4
	s_mov_b32 s34, 0x4bda12f7
	s_mov_b32 s35, 0x2aaaaaab
	s_add_i32 s36, s32, 48
	s_mul_i32 s37, s36, 48
	s_mul_hi_u32 s38, s37, s34
	s_lshr_b32 s38, s38, 3
	s_add_i32 s39, s37, 47
	s_mul_hi_u32 s39, s39, s34
	s_lshr_b32 s39, s39, 3
	s_add_i32 s40, s38, 1
	s_mul_i32 s41, s38, 27
	s_mul_hi_u32 s41, s41, s35
	s_lshr_b32 s41, s41, 3
	s_cmp_lg_u32 s41, s36
	s_cselect_b32 s41, 1, 0
	s_lshl_b32 s42, s38, 1
	s_add_i32 s42, s42, s41
	s_lshl_b32 s42, s42, 6
	s_add_i32 s42, s42, s33
	s_lshl_b32 s43, s42, 9
	s_add_u32 s44, s4, s43
	s_addc_u32 s45, s5, 0
	global_load_dwordx4 v[132:135], v130, s[44:45]
	global_load_dwordx4 v[132:135], v130, s[44:45] offset:64
	s_lshl_b32 s43, s42, 4
	s_add_u32 s44, s6, s43
	s_addc_u32 s45, s7, 0
	global_load_dword v132, v131, s[44:45]
	s_mul_i32 s41, s40, 27
	s_mul_hi_u32 s41, s41, s35
	s_lshr_b32 s41, s41, 3
	s_cmp_lg_u32 s41, s36
	s_cselect_b32 s41, 1, 0
	s_lshl_b32 s42, s40, 1
	s_add_i32 s42, s42, s41
	s_lshl_b32 s42, s42, 6
	s_add_i32 s42, s42, s33
	s_lshl_b32 s43, s42, 9
	s_add_u32 s44, s4, s43
	s_addc_u32 s45, s5, 0
	global_load_dwordx4 v[132:135], v130, s[44:45]
	global_load_dwordx4 v[132:135], v130, s[44:45] offset:64
	s_lshl_b32 s43, s42, 4
	s_add_u32 s44, s6, s43
	s_addc_u32 s45, s7, 0
	global_load_dword v132, v131, s[44:45]
	s_mul_i32 s41, s39, 27
	s_mul_hi_u32 s41, s41, s35
	s_lshr_b32 s41, s41, 3
	s_cmp_lg_u32 s41, s36
	s_cselect_b32 s41, 1, 0
	s_lshl_b32 s42, s39, 1
	s_add_i32 s42, s42, s41
	s_lshl_b32 s42, s42, 6
	s_add_i32 s42, s42, s33
	s_lshl_b32 s43, s42, 9
	s_add_u32 s44, s4, s43
	s_addc_u32 s45, s5, 0
	global_load_dwordx4 v[132:135], v130, s[44:45]
	global_load_dwordx4 v[132:135], v130, s[44:45] offset:64
	s_lshl_b32 s43, s42, 4
	s_add_u32 s44, s6, s43
	s_addc_u32 s45, s7, 0
	global_load_dword v132, v131, s[44:45]
	s_add_i32 s36, s32, 96
	s_mul_i32 s37, s36, 48
	s_mul_hi_u32 s38, s37, s34
	s_lshr_b32 s38, s38, 3
	s_add_i32 s39, s37, 47
	s_mul_hi_u32 s39, s39, s34
	s_lshr_b32 s39, s39, 3
	s_add_i32 s40, s38, 1
	s_mul_i32 s41, s38, 27
	s_mul_hi_u32 s41, s41, s35
	s_lshr_b32 s41, s41, 3
	s_cmp_lg_u32 s41, s36
	s_cselect_b32 s41, 1, 0
	s_lshl_b32 s42, s38, 1
	s_add_i32 s42, s42, s41
	s_lshl_b32 s42, s42, 6
	s_add_i32 s42, s42, s33
	s_lshl_b32 s43, s42, 9
	s_add_u32 s44, s4, s43
	s_addc_u32 s45, s5, 0
	global_load_dwordx4 v[132:135], v130, s[44:45]
	global_load_dwordx4 v[132:135], v130, s[44:45] offset:64
	s_lshl_b32 s43, s42, 4
	s_add_u32 s44, s6, s43
	s_addc_u32 s45, s7, 0
	global_load_dword v132, v131, s[44:45]
	s_mul_i32 s41, s40, 27
	s_mul_hi_u32 s41, s41, s35
	s_lshr_b32 s41, s41, 3
	s_cmp_lg_u32 s41, s36
	s_cselect_b32 s41, 1, 0
	s_lshl_b32 s42, s40, 1
	s_add_i32 s42, s42, s41
	s_lshl_b32 s42, s42, 6
	s_add_i32 s42, s42, s33
	s_lshl_b32 s43, s42, 9
	s_add_u32 s44, s4, s43
	s_addc_u32 s45, s5, 0
	global_load_dwordx4 v[132:135], v130, s[44:45]
	global_load_dwordx4 v[132:135], v130, s[44:45] offset:64
	s_lshl_b32 s43, s42, 4
	s_add_u32 s44, s6, s43
	s_addc_u32 s45, s7, 0
	global_load_dword v132, v131, s[44:45]
	s_mul_i32 s41, s39, 27
	s_mul_hi_u32 s41, s41, s35
	s_lshr_b32 s41, s41, 3
	s_cmp_lg_u32 s41, s36
	s_cselect_b32 s41, 1, 0
	s_lshl_b32 s42, s39, 1
	s_add_i32 s42, s42, s41
	s_lshl_b32 s42, s42, 6
	s_add_i32 s42, s42, s33
	s_lshl_b32 s43, s42, 9
	s_add_u32 s44, s4, s43
	s_addc_u32 s45, s5, 0
	global_load_dwordx4 v[132:135], v130, s[44:45]
	global_load_dwordx4 v[132:135], v130, s[44:45] offset:64
	s_lshl_b32 s43, s42, 4
	s_add_u32 s44, s6, s43
	s_addc_u32 s45, s7, 0
	global_load_dword v132, v131, s[44:45]
	s_mov_b32 s30, 0
	v_readfirstlane_b32 s24, v1
	s_cmp_lg_u32 s2, 0xbf
	s_cbranch_scc1 .Lk3_l1skipB
	s_cmp_lg_u32 s24, 3
	s_cbranch_scc1 .Lk3_l1skipB
	s_mov_b32 s30, 1
	v_and_b32_e32 v124, 63, v0
	v_lshlrev_b32_e32 v124, 2, v124
	global_load_dword v112, v124, s[20:21]
	global_load_dword v113, v124, s[20:21] offset:256
	global_load_dword v114, v124, s[20:21] offset:512
	global_load_dword v115, v124, s[20:21] offset:768
	global_load_dword v116, v124, s[20:21] offset:1024
	global_load_dword v117, v124, s[20:21] offset:1280
	global_load_dword v118, v124, s[20:21] offset:1536
	global_load_dword v119, v124, s[20:21] offset:1792
	global_load_dword v120, v124, s[20:21] offset:2048
	global_load_dword v121, v124, s[20:21] offset:2304
	global_load_dword v122, v124, s[20:21] offset:2560
	global_load_dword v123, v124, s[20:21] offset:2816

	.amdhsa_kernel _Z10epi_kernelPKDF16_PKfS2_S2_S2_S2_Pf
		.amdhsa_group_segment_fixed_size 16192
		.amdhsa_private_segment_fixed_size 0
		.amdhsa_kernarg_size 56
		.amdhsa_user_sgpr_count 2
		.amdhsa_user_sgpr_dispatch_ptr 0
		.amdhsa_user_sgpr_queue_ptr 0
		.amdhsa_user_sgpr_kernarg_segment_ptr 1
		.amdhsa_user_sgpr_dispatch_id 0
		.amdhsa_user_sgpr_kernarg_preload_length 0
		.amdhsa_user_sgpr_kernarg_preload_offset 0
		.amdhsa_user_sgpr_private_segment_size 0
		.amdhsa_uses_dynamic_stack 0
		.amdhsa_enable_private_segment 0
		.amdhsa_system_sgpr_workgroup_id_x 1
		.amdhsa_system_sgpr_workgroup_id_y 0
		.amdhsa_system_sgpr_workgroup_id_z 0
		.amdhsa_system_sgpr_workgroup_info 0
		.amdhsa_system_vgpr_workitem_id 0
		.amdhsa_next_free_vgpr 172
		.amdhsa_next_free_sgpr 64
		.amdhsa_accum_offset 160
		.amdhsa_reserve_vcc 1
		.amdhsa_float_round_mode_32 0
		.amdhsa_float_round_mode_16_64 0
		.amdhsa_float_denorm_mode_32 3
		.amdhsa_float_denorm_mode_16_64 3
		.amdhsa_dx10_clamp 1
		.amdhsa_ieee_mode 1
		.amdhsa_fp16_overflow 0
		.amdhsa_tg_split 0
		.amdhsa_exception_fp_ieee_invalid_op 0
		.amdhsa_exception_fp_denorm_src 0
		.amdhsa_exception_fp_ieee_div_zero 0
		.amdhsa_exception_fp_ieee_overflow 0
		.amdhsa_exception_fp_ieee_underflow 0
		.amdhsa_exception_fp_ieee_inexact 0
		.amdhsa_exception_int_div_zero 0
	.end_amdhsa_kernel

amdhsa.kernels:
  - .agpr_count:     0
    .args:
      - .actual_access:  read_only
        .address_space:  global
        .offset:         0
        .size:           8
        .value_kind:     global_buffer
      - .actual_access:  read_only
        .address_space:  global
        .offset:         8
        .size:           8
        .value_kind:     global_buffer
      - .actual_access:  read_only
        .address_space:  global
        .offset:         16
        .size:           8
        .value_kind:     global_buffer
      - .actual_access:  write_only
        .address_space:  global
        .offset:         24
        .size:           8
        .value_kind:     global_buffer
      - .actual_access:  write_only
        .address_space:  global
        .offset:         32
        .size:           8
        .value_kind:     global_buffer
      - .actual_access:  write_only
        .address_space:  global
        .offset:         40
        .size:           8
        .value_kind:     global_buffer
    .group_segment_fixed_size: 57344
    .kernarg_segment_align: 8
    .kernarg_segment_size: 48
    .language:       OpenCL C
    .language_version:
      - 2
      - 0
    .max_flat_workgroup_size: 512
    .name:           _Z12gemm1_kernelPKfS0_S0_PDv8_DF16_PDF16_S3_
    .private_segment_fixed_size: 0
    .sgpr_count:     18
    .sgpr_spill_count: 0
    .symbol:         _Z12gemm1_kernelPKfS0_S0_PDv8_DF16_PDF16_S3_.kd
    .uniform_work_group_size: 1
    .uses_dynamic_stack: false
    .vgpr_count:     125
    .vgpr_spill_count: 0
    .wavefront_size: 64
  - .agpr_count:     0
    .args:
      - .actual_access:  read_only
        .address_space:  global
        .offset:         0
        .size:           8
        .value_kind:     global_buffer
      - .actual_access:  read_only
        .address_space:  global
        .offset:         8
        .size:           8
        .value_kind:     global_buffer
      - .actual_access:  read_only
        .address_space:  global
        .offset:         16
        .size:           8
        .value_kind:     global_buffer
      - .actual_access:  read_only
        .address_space:  global
        .offset:         24
        .size:           8
        .value_kind:     global_buffer
      - .actual_access:  write_only
        .address_space:  global
        .offset:         32
        .size:           8
        .value_kind:     global_buffer
      - .actual_access:  write_only
        .address_space:  global
        .offset:         40
        .size:           8
        .value_kind:     global_buffer
    .group_segment_fixed_size: 87040
    .kernarg_segment_align: 8
    .kernarg_segment_size: 48
    .language:       OpenCL C
    .language_version:
      - 2
      - 0
    .max_flat_workgroup_size: 768
    .name:           _Z11attn_kernelPKiPKDv8_DF16_PKDF16_S5_PDF16_Pf
    .private_segment_fixed_size: 0
    .sgpr_count:     55
    .sgpr_spill_count: 0
    .symbol:         _Z11attn_kernelPKiPKDv8_DF16_PKDF16_S5_PDF16_Pf.kd
    .uniform_work_group_size: 1
    .uses_dynamic_stack: false
    .vgpr_count:     156
    .vgpr_spill_count: 0
    .wavefront_size: 64
  - .agpr_count:     12
    .args:
      - .actual_access:  read_only
        .address_space:  global
        .offset:         0
        .size:           8
        .value_kind:     global_buffer
      - .actual_access:  read_only
        .address_space:  global
        .offset:         8
        .size:           8
        .value_kind:     global_buffer
      - .actual_access:  read_only
        .address_space:  global
        .offset:         16
        .size:           8
        .value_kind:     global_buffer
      - .actual_access:  read_only
        .address_space:  global
        .offset:         24
        .size:           8
        .value_kind:     global_buffer
      - .actual_access:  read_only
        .address_space:  global
        .offset:         32
        .size:           8
        .value_kind:     global_buffer
      - .actual_access:  read_only
        .address_space:  global
        .offset:         40
        .size:           8
        .value_kind:     global_buffer
      - .actual_access:  write_only
        .address_space:  global
        .offset:         48
        .size:           8
        .value_kind:     global_buffer
    .group_segment_fixed_size: 16192
    .kernarg_segment_align: 8
    .kernarg_segment_size: 56
    .language:       OpenCL C
    .language_version:
      - 2
      - 0
    .max_flat_workgroup_size: 256
    .name:           _Z10epi_kernelPKDF16_PKfS2_S2_S2_S2_Pf
    .private_segment_fixed_size: 0
    .sgpr_count:     70
    .sgpr_spill_count: 0
    .symbol:         _Z10epi_kernelPKDF16_PKfS2_S2_S2_S2_Pf.kd
    .uniform_work_group_size: 1
    .uses_dynamic_stack: false
    .vgpr_count:     172
    .vgpr_spill_count: 0
    .wavefront_size: 64
